# A-tile LDS-DMA issues moved from the first four MFMA groups to the top of the K-tile (behind the first LDS reads) in the MoE gate/up main K-loop
# baseline (speedup 1.0000x reference)
.LBB0_1433:
	s_add_i32 s88, s39, 0xffff8000
	s_and_b32 s88, s88, 0x8000
	s_add_i32 s88, s88, 0
	s_add_i32 s87, s86, 0
	s_add_i32 s88, s88, 0x18000
	v_add_u32_e32 v246, s88, v212
	v_add_u32_e32 v247, s87, v215
	v_add_u32_e32 v252, s88, v181
	v_add_u32_e32 v254, s88, v172
	v_add_u32_e32 v250, s88, v183
	ds_read_b64_tr_b16 v[222:223], v246
	ds_read_b64_tr_b16 v[224:225], v246 offset:2048
	ds_read_b64_tr_b16 v[226:227], v250
	ds_read_b64_tr_b16 v[228:229], v250 offset:2048
	ds_read_b128 v[162:165], v247
	ds_read_b128 v[166:169], v247 offset:2048
	ds_read_b64_tr_b16 v[230:231], v252
	ds_read_b64_tr_b16 v[232:233], v252 offset:2048
	ds_read_b64_tr_b16 v[234:235], v254
	ds_read_b64_tr_b16 v[236:237], v254 offset:2048
	s_add_i32 s89, s38, s85
	s_mov_b32 s90, m0
	s_mov_b32 m0, s89
	s_nop 0
	global_load_lds_dwordx4 v221, s[18:19]
	s_mov_b32 m0, s90
	s_add_i32 s90, s89, 0x2000
	s_mov_b32 s91, m0
	s_mov_b32 m0, s90
	s_nop 0
	global_load_lds_dwordx4 v220, s[18:19]
	s_mov_b32 m0, s91
	s_add_i32 s90, s89, 0x4000
	s_mov_b32 s91, m0
	s_mov_b32 m0, s90
	s_nop 0
	global_load_lds_dwordx4 v219, s[18:19]
	s_mov_b32 m0, s91
	s_addk_i32 s89, 0x6000
	s_mov_b32 s90, m0
	s_mov_b32 m0, s89
	s_nop 0
	global_load_lds_dwordx4 v218, s[18:19]
	s_mov_b32 m0, s90
	s_waitcnt lgkmcnt(5)
	v_mfma_f32_16x16x32_bf16 v[62:65], v[222:225], v[162:165], v[62:65]
	ds_read_b128 v[238:241], v247 offset:4096
	s_and_b32 s88, s39, 0x8000
	v_mfma_f32_16x16x32_bf16 v[58:61], v[226:229], v[162:165], v[58:61]
	s_waitcnt lgkmcnt(3)
	v_mfma_f32_16x16x32_bf16 v[54:57], v[230:233], v[162:165], v[54:57]
	s_waitcnt lgkmcnt(1)
	v_mfma_f32_16x16x32_bf16 v[42:45], v[234:237], v[162:165], v[42:45]
	v_mfma_f32_16x16x32_bf16 v[50:53], v[222:225], v[166:169], v[50:53]
	ds_read_b128 v[162:165], v247 offset:6144
	v_mfma_f32_16x16x32_bf16 v[46:49], v[226:229], v[166:169], v[46:49]
	v_mfma_f32_16x16x32_bf16 v[38:41], v[230:233], v[166:169], v[38:41]
	v_mfma_f32_16x16x32_bf16 v[34:37], v[234:237], v[166:169], v[34:37]
	s_waitcnt lgkmcnt(1)
	v_mfma_f32_16x16x32_bf16 v[66:69], v[222:225], v[238:241], v[66:69]
	ds_read_b128 v[166:169], v247 offset:8192
	v_mfma_f32_16x16x32_bf16 v[70:73], v[226:229], v[238:241], v[70:73]
	v_mfma_f32_16x16x32_bf16 v[74:77], v[230:233], v[238:241], v[74:77]
	v_mfma_f32_16x16x32_bf16 v[78:81], v[234:237], v[238:241], v[78:81]
	s_waitcnt lgkmcnt(1)
	v_mfma_f32_16x16x32_bf16 v[82:85], v[222:225], v[162:165], v[82:85]
	ds_read_b128 v[238:241], v247 offset:10240
	v_mfma_f32_16x16x32_bf16 v[86:89], v[226:229], v[162:165], v[86:89]
	v_mfma_f32_16x16x32_bf16 v[90:93], v[230:233], v[162:165], v[90:93]
	v_mfma_f32_16x16x32_bf16 v[94:97], v[234:237], v[162:165], v[94:97]
	ds_read_b128 v[242:245], v247 offset:12288
	ds_read_b64_tr_b16 v[162:163], v246 offset:16384
	ds_read_b64_tr_b16 v[164:165], v246 offset:18432
	s_waitcnt lgkmcnt(4)
	v_mfma_f32_16x16x32_bf16 v[98:101], v[222:225], v[166:169], v[98:101]
	v_mfma_f32_16x16x32_bf16 v[102:105], v[226:229], v[166:169], v[102:105]
	v_mfma_f32_16x16x32_bf16 v[106:109], v[230:233], v[166:169], v[106:109]
	v_mfma_f32_16x16x32_bf16 v[110:113], v[234:237], v[166:169], v[110:113]
	ds_read_b128 v[246:249], v247 offset:14336
	ds_read_b64_tr_b16 v[166:167], v250 offset:16384
	ds_read_b64_tr_b16 v[168:169], v250 offset:18432
	s_waitcnt lgkmcnt(6)
	v_mfma_f32_16x16x32_bf16 v[114:117], v[222:225], v[238:241], v[114:117]
	v_mfma_f32_16x16x32_bf16 v[118:121], v[226:229], v[238:241], v[118:121]
	v_mfma_f32_16x16x32_bf16 v[122:125], v[230:233], v[238:241], v[122:125]
	v_mfma_f32_16x16x32_bf16 v[126:129], v[234:237], v[238:241], v[126:129]
	v_add_u32_e32 v200, s87, v216
	ds_read_b128 v[238:241], v200
	ds_read_b64_tr_b16 v[250:251], v252 offset:16384
	ds_read_b64_tr_b16 v[252:253], v252 offset:18432
	s_waitcnt lgkmcnt(8)
	v_mfma_f32_16x16x32_bf16 v[130:133], v[222:225], v[242:245], v[130:133]
	v_mfma_f32_16x16x32_bf16 v[134:137], v[226:229], v[242:245], v[134:137]
	v_mfma_f32_16x16x32_bf16 v[138:141], v[230:233], v[242:245], v[138:141]
	v_mfma_f32_16x16x32_bf16 v[142:145], v[234:237], v[242:245], v[142:145]
	s_waitcnt lgkmcnt(5)
	v_mfma_f32_16x16x32_bf16 v[146:149], v[222:225], v[246:249], v[146:149]
	v_mfma_f32_16x16x32_bf16 v[150:153], v[226:229], v[246:249], v[150:153]
	ds_read_b128 v[222:225], v200 offset:2048
	ds_read_b64_tr_b16 v[226:227], v254 offset:16384
	ds_read_b64_tr_b16 v[228:229], v254 offset:18432
	v_mfma_f32_16x16x32_bf16 v[154:157], v[230:233], v[246:249], v[154:157]
	v_mfma_f32_16x16x32_bf16 v[158:161], v[234:237], v[246:249], v[158:161]
	ds_read_b128 v[230:233], v200 offset:4096
	s_waitcnt lgkmcnt(6)
	v_mfma_f32_16x16x32_bf16 v[62:65], v[162:165], v[238:241], v[62:65]
	s_add_u32 s87, s83, s2
	s_waitcnt vmcnt(11)
	s_addc_u32 s90, s84, s3
	v_mfma_f32_16x16x32_bf16 v[58:61], v[166:169], v[238:241], v[58:61]
	v_cvt_pk_bf16_f32 v30, v30, v31
	v_cvt_pk_bf16_f32 v31, v32, v33
	v_add_u32_e32 v242, s88, v217
	s_waitcnt lgkmcnt(4)
	v_mfma_f32_16x16x32_bf16 v[54:57], v[250:253], v[238:241], v[54:57]
	s_add_u32 s88, s87, 0x160000
	ds_write_b64 v242, v[30:31]
	s_addc_u32 s89, s90, 0
	s_waitcnt lgkmcnt(2)
	v_mfma_f32_16x16x32_bf16 v[42:45], v[226:229], v[238:241], v[42:45]
	global_load_dwordx4 v[30:33], v199, s[88:89]
	v_mfma_f32_16x16x32_bf16 v[50:53], v[162:165], v[222:225], v[50:53]
	ds_read_b128 v[234:237], v200 offset:6144
	s_waitcnt vmcnt(11)
	s_add_u32 s88, s87, 0x18c000
	v_mfma_f32_16x16x32_bf16 v[46:49], v[166:169], v[222:225], v[46:49]
	v_cvt_pk_bf16_f32 v26, v26, v27
	v_cvt_pk_bf16_f32 v27, v28, v29
	ds_write_b64 v242, v[26:27] offset:8192
	v_mfma_f32_16x16x32_bf16 v[38:41], v[250:253], v[222:225], v[38:41]
	s_addc_u32 s89, s90, 0
	global_load_dwordx4 v[26:29], v199, s[88:89]
	v_mfma_f32_16x16x32_bf16 v[34:37], v[226:229], v[222:225], v[34:37]
	s_waitcnt lgkmcnt(3)
	v_mfma_f32_16x16x32_bf16 v[66:69], v[162:165], v[230:233], v[66:69]
	ds_read_b128 v[222:225], v200 offset:8192
	s_waitcnt vmcnt(11)
	s_add_u32 s88, s87, 0x1b8000
	v_mfma_f32_16x16x32_bf16 v[70:73], v[166:169], v[230:233], v[70:73]
	v_cvt_pk_bf16_f32 v22, v22, v23
	v_cvt_pk_bf16_f32 v23, v24, v25
	ds_write_b64 v242, v[22:23] offset:16384
	v_mfma_f32_16x16x32_bf16 v[74:77], v[250:253], v[230:233], v[74:77]
	s_addc_u32 s89, s90, 0
	global_load_dwordx4 v[22:25], v199, s[88:89]
	v_mfma_f32_16x16x32_bf16 v[78:81], v[226:229], v[230:233], v[78:81]
	s_waitcnt lgkmcnt(3)
	v_mfma_f32_16x16x32_bf16 v[82:85], v[162:165], v[234:237], v[82:85]
	ds_read_b128 v[230:233], v200 offset:10240
	s_waitcnt vmcnt(11)
	s_add_u32 s88, s87, 0x1e4000
	v_mfma_f32_16x16x32_bf16 v[86:89], v[166:169], v[234:237], v[86:89]
	v_cvt_pk_bf16_f32 v18, v18, v19
	v_cvt_pk_bf16_f32 v19, v20, v21
	ds_write_b64 v242, v[18:19] offset:24576
	v_mfma_f32_16x16x32_bf16 v[90:93], v[250:253], v[234:237], v[90:93]
	s_addc_u32 s89, s90, 0
	global_load_dwordx4 v[18:21], v199, s[88:89]
	v_mfma_f32_16x16x32_bf16 v[94:97], v[226:229], v[234:237], v[94:97]
	ds_read_b128 v[234:237], v200 offset:12288
	s_waitcnt lgkmcnt(4)
	v_mfma_f32_16x16x32_bf16 v[98:101], v[162:165], v[222:225], v[98:101]
	s_add_u32 s87, s40, s2
	s_waitcnt vmcnt(11)
	s_addc_u32 s90, s41, s3
	v_mfma_f32_16x16x32_bf16 v[102:105], v[166:169], v[222:225], v[102:105]
	v_cvt_pk_bf16_f32 v14, v14, v15
	v_cvt_pk_bf16_f32 v15, v16, v17
	s_add_u32 s88, s87, 0x160000
	v_mfma_f32_16x16x32_bf16 v[106:109], v[250:253], v[222:225], v[106:109]
	ds_write_b64 v242, v[14:15] offset:256
	s_addc_u32 s89, s90, 0
	global_load_dwordx4 v[14:17], v199, s[88:89]
	v_mfma_f32_16x16x32_bf16 v[110:113], v[226:229], v[222:225], v[110:113]
	s_waitcnt lgkmcnt(3)
	v_mfma_f32_16x16x32_bf16 v[114:117], v[162:165], v[230:233], v[114:117]
	ds_read_b128 v[222:225], v200 offset:14336
	s_waitcnt vmcnt(11)
	s_add_u32 s88, s87, 0x18c000
	v_mfma_f32_16x16x32_bf16 v[118:121], v[166:169], v[230:233], v[118:121]
	v_cvt_pk_bf16_f32 v10, v10, v11
	v_cvt_pk_bf16_f32 v11, v12, v13
	ds_write_b64 v242, v[10:11] offset:8448
	v_mfma_f32_16x16x32_bf16 v[122:125], v[250:253], v[230:233], v[122:125]
	s_addc_u32 s89, s90, 0
	global_load_dwordx4 v[10:13], v199, s[88:89]
	v_mfma_f32_16x16x32_bf16 v[126:129], v[226:229], v[230:233], v[126:129]
	s_waitcnt lgkmcnt(3)
	v_mfma_f32_16x16x32_bf16 v[130:133], v[162:165], v[234:237], v[130:133]
	s_waitcnt vmcnt(11)
	s_add_u32 s88, s87, 0x1b8000
	v_cvt_pk_bf16_f32 v6, v6, v7
	v_mfma_f32_16x16x32_bf16 v[134:137], v[166:169], v[234:237], v[134:137]
	v_cvt_pk_bf16_f32 v7, v8, v9
	ds_write_b64 v242, v[6:7] offset:16640
	s_addc_u32 s89, s90, 0
	v_mfma_f32_16x16x32_bf16 v[138:141], v[250:253], v[234:237], v[138:141]
	global_load_dwordx4 v[6:9], v199, s[88:89]
	v_mfma_f32_16x16x32_bf16 v[142:145], v[226:229], v[234:237], v[142:145]
	s_waitcnt lgkmcnt(2)
	v_mfma_f32_16x16x32_bf16 v[146:149], v[162:165], v[222:225], v[146:149]
	s_waitcnt vmcnt(11)
	s_add_u32 s88, s87, 0x1e4000
	v_cvt_pk_bf16_f32 v2, v2, v3
	v_mfma_f32_16x16x32_bf16 v[150:153], v[166:169], v[222:225], v[150:153]
	v_cvt_pk_bf16_f32 v3, v4, v5
	ds_write_b64 v242, v[2:3] offset:24832
	s_addc_u32 s89, s90, 0
	v_mfma_f32_16x16x32_bf16 v[154:157], v[250:253], v[222:225], v[154:157]
	global_load_dwordx4 v[2:5], v199, s[88:89]
	v_mfma_f32_16x16x32_bf16 v[158:161], v[226:229], v[222:225], v[158:161]
	s_add_i32 s87, s86, 0x8000
	s_cmp_lg_u32 s86, 0x10000
	s_cselect_b32 s86, s87, 0
	s_add_i32 s87, s85, 0x8000
	s_cmp_lg_u32 s85, 0x10000
	s_waitcnt lgkmcnt(0)
	s_barrier
	s_cselect_b32 s85, s87, 0
	s_add_u32 s2, s2, 0xb0000
	s_addc_u32 s3, s3, 0
	s_add_i32 s39, s39, 0x8000
	v_add_u32_e32 v218, 0x80, v218
	v_add_u32_e32 v219, 0x80, v219
	v_add_u32_e32 v220, 0x80, v220
	s_cmp_lg_u32 s2, 0x14a0000
	v_add_u32_e32 v221, 0x80, v221
	s_cbranch_scc1 .LBB0_1433
	v_add_u32_e32 v200, s52, v212
	v_add_u32_e32 v250, 0, v215
	v_add_u32_e32 v215, s52, v181
	v_add_u32_e32 v251, s52, v172
	v_add_u32_e32 v217, s52, v183
	ds_read_b64_tr_b16 v[162:163], v200
	ds_read_b64_tr_b16 v[164:165], v200 offset:2048
	ds_read_b64_tr_b16 v[166:167], v217
	ds_read_b64_tr_b16 v[168:169], v217 offset:2048
	ds_read_b128 v[218:221], v250
	ds_read_b128 v[222:225], v250 offset:2048
	ds_read_b64_tr_b16 v[226:227], v215
	ds_read_b64_tr_b16 v[228:229], v215 offset:2048
	ds_read_b64_tr_b16 v[230:231], v251
	ds_read_b64_tr_b16 v[232:233], v251 offset:2048
	s_waitcnt lgkmcnt(5)
	v_mfma_f32_16x16x32_bf16 v[62:65], v[162:165], v[218:221], v[62:65]
	ds_read_b128 v[234:237], v250 offset:4096
	v_mfma_f32_16x16x32_bf16 v[58:61], v[166:169], v[218:221], v[58:61]
	s_waitcnt lgkmcnt(3)
	v_mfma_f32_16x16x32_bf16 v[54:57], v[226:229], v[218:221], v[54:57]
	s_waitcnt lgkmcnt(1)
	v_mfma_f32_16x16x32_bf16 v[42:45], v[230:233], v[218:221], v[42:45]
	v_mfma_f32_16x16x32_bf16 v[50:53], v[162:165], v[222:225], v[50:53]
	ds_read_b128 v[218:221], v250 offset:6144
	v_mfma_f32_16x16x32_bf16 v[46:49], v[166:169], v[222:225], v[46:49]
	v_mfma_f32_16x16x32_bf16 v[38:41], v[226:229], v[222:225], v[38:41]
	v_mfma_f32_16x16x32_bf16 v[34:37], v[230:233], v[222:225], v[34:37]
	s_waitcnt lgkmcnt(1)
	v_mfma_f32_16x16x32_bf16 v[66:69], v[162:165], v[234:237], v[66:69]
	ds_read_b128 v[222:225], v250 offset:8192
	v_mfma_f32_16x16x32_bf16 v[70:73], v[166:169], v[234:237], v[70:73]
	v_mfma_f32_16x16x32_bf16 v[74:77], v[226:229], v[234:237], v[74:77]
	v_mfma_f32_16x16x32_bf16 v[78:81], v[230:233], v[234:237], v[78:81]
	s_waitcnt lgkmcnt(1)
	v_mfma_f32_16x16x32_bf16 v[82:85], v[162:165], v[218:221], v[82:85]
	ds_read_b128 v[234:237], v250 offset:10240
	v_mfma_f32_16x16x32_bf16 v[86:89], v[166:169], v[218:221], v[86:89]
	v_mfma_f32_16x16x32_bf16 v[90:93], v[226:229], v[218:221], v[90:93]
	v_mfma_f32_16x16x32_bf16 v[94:97], v[230:233], v[218:221], v[94:97]
	ds_read_b128 v[218:221], v250 offset:12288
	ds_read_b64_tr_b16 v[238:239], v200 offset:16384
	ds_read_b64_tr_b16 v[240:241], v200 offset:18432
	s_waitcnt lgkmcnt(4)
	v_mfma_f32_16x16x32_bf16 v[98:101], v[162:165], v[222:225], v[98:101]
	v_mfma_f32_16x16x32_bf16 v[102:105], v[166:169], v[222:225], v[102:105]
	v_mfma_f32_16x16x32_bf16 v[106:109], v[226:229], v[222:225], v[106:109]
	v_mfma_f32_16x16x32_bf16 v[110:113], v[230:233], v[222:225], v[110:113]
	ds_read_b128 v[222:225], v250 offset:14336
	ds_read_b64_tr_b16 v[242:243], v217 offset:16384
	ds_read_b64_tr_b16 v[244:245], v217 offset:18432
	s_waitcnt lgkmcnt(6)
	v_mfma_f32_16x16x32_bf16 v[114:117], v[162:165], v[234:237], v[114:117]
	v_mfma_f32_16x16x32_bf16 v[118:121], v[166:169], v[234:237], v[118:121]
	v_mfma_f32_16x16x32_bf16 v[122:125], v[226:229], v[234:237], v[122:125]
	v_mfma_f32_16x16x32_bf16 v[126:129], v[230:233], v[234:237], v[126:129]
	v_add_u32_e32 v200, 0, v216
	ds_read_b128 v[234:237], v200
	ds_read_b64_tr_b16 v[246:247], v215 offset:16384
	ds_read_b64_tr_b16 v[248:249], v215 offset:18432
	s_waitcnt lgkmcnt(8)
	v_mfma_f32_16x16x32_bf16 v[130:133], v[162:165], v[218:221], v[130:133]
	v_mfma_f32_16x16x32_bf16 v[134:137], v[166:169], v[218:221], v[134:137]
	v_mfma_f32_16x16x32_bf16 v[138:141], v[226:229], v[218:221], v[138:141]
	v_mfma_f32_16x16x32_bf16 v[142:145], v[230:233], v[218:221], v[142:145]
	s_waitcnt lgkmcnt(5)
	v_mfma_f32_16x16x32_bf16 v[146:149], v[162:165], v[222:225], v[146:149]
	v_mfma_f32_16x16x32_bf16 v[150:153], v[166:169], v[222:225], v[150:153]
	ds_read_b128 v[162:165], v200 offset:2048
	ds_read_b64_tr_b16 v[166:167], v251 offset:16384
	ds_read_b64_tr_b16 v[168:169], v251 offset:18432
	v_mfma_f32_16x16x32_bf16 v[154:157], v[226:229], v[222:225], v[154:157]
	v_mfma_f32_16x16x32_bf16 v[158:161], v[230:233], v[222:225], v[158:161]
	ds_read_b128 v[216:219], v200 offset:4096
	s_waitcnt vmcnt(7)
	v_add_u32_e32 v214, s56, v214
	v_cvt_pk_bf16_f32 v30, v30, v31
	v_cvt_pk_bf16_f32 v31, v32, v33
	s_waitcnt lgkmcnt(6)
	v_mfma_f32_16x16x32_bf16 v[62:65], v[238:241], v[234:237], v[62:65]
	ds_write_b64 v214, v[30:31]
	v_mfma_f32_16x16x32_bf16 v[58:61], v[242:245], v[234:237], v[58:61]
	s_waitcnt lgkmcnt(5)
	v_mfma_f32_16x16x32_bf16 v[54:57], v[246:249], v[234:237], v[54:57]
	s_waitcnt lgkmcnt(2)
	v_mfma_f32_16x16x32_bf16 v[30:33], v[166:169], v[234:237], v[42:45]
	v_mfma_f32_16x16x32_bf16 v[42:45], v[238:241], v[162:165], v[50:53]
	s_nop 2
	ds_read_b128 v[50:53], v200 offset:6144
	s_waitcnt vmcnt(6)
	v_mfma_f32_16x16x32_bf16 v[46:49], v[242:245], v[162:165], v[46:49]
	v_cvt_pk_bf16_f32 v26, v26, v27
	v_cvt_pk_bf16_f32 v27, v28, v29
	ds_write_b64 v214, v[26:27] offset:8192
	v_mfma_f32_16x16x32_bf16 v[38:41], v[246:249], v[162:165], v[38:41]
	v_mfma_f32_16x16x32_bf16 v[26:29], v[166:169], v[162:165], v[34:37]
	s_waitcnt lgkmcnt(3)
	v_mfma_f32_16x16x32_bf16 v[34:37], v[238:241], v[216:219], v[66:69]
	v_mfma_f32_16x16x32_bf16 v[66:69], v[242:245], v[216:219], v[70:73]
	s_nop 2
	ds_read_b128 v[70:73], v200 offset:8192
	s_waitcnt vmcnt(5)
	v_mfma_f32_16x16x32_bf16 v[74:77], v[246:249], v[216:219], v[74:77]
	v_cvt_pk_bf16_f32 v22, v22, v23
	v_cvt_pk_bf16_f32 v23, v24, v25
	ds_write_b64 v214, v[22:23] offset:16384
	v_mfma_f32_16x16x32_bf16 v[22:25], v[166:169], v[216:219], v[78:81]
	s_waitcnt lgkmcnt(3)
	v_mfma_f32_16x16x32_bf16 v[78:81], v[238:241], v[50:53], v[82:85]
	v_mfma_f32_16x16x32_bf16 v[82:85], v[242:245], v[50:53], v[86:89]
	s_nop 2
	ds_read_b128 v[86:89], v200 offset:10240
	s_waitcnt vmcnt(4)
	v_mfma_f32_16x16x32_bf16 v[90:93], v[246:249], v[50:53], v[90:93]
	v_cvt_pk_bf16_f32 v18, v18, v19
	v_cvt_pk_bf16_f32 v19, v20, v21
	ds_write_b64 v214, v[18:19] offset:24576
	v_mfma_f32_16x16x32_bf16 v[18:21], v[166:169], v[50:53], v[94:97]
	s_waitcnt lgkmcnt(3)
	v_mfma_f32_16x16x32_bf16 v[50:53], v[238:241], v[70:73], v[98:101]
	v_add_u32_e32 v162, s56, v213
	s_nop 1
	ds_read_b128 v[98:101], v200 offset:12288
	s_waitcnt vmcnt(3)
	v_mfma_f32_16x16x32_bf16 v[94:97], v[242:245], v[70:73], v[102:105]
	v_cvt_pk_bf16_f32 v14, v14, v15
	v_cvt_pk_bf16_f32 v15, v16, v17
	ds_write_b64 v162, v[14:15]
	v_mfma_f32_16x16x32_bf16 v[102:105], v[246:249], v[70:73], v[106:109]
	v_mfma_f32_16x16x32_bf16 v[14:17], v[166:169], v[70:73], v[110:113]
	s_nop 2
	ds_read_b128 v[110:113], v200 offset:14336
	s_waitcnt vmcnt(2)
	s_waitcnt lgkmcnt(4)
	v_mfma_f32_16x16x32_bf16 v[70:73], v[238:241], v[86:89], v[114:117]
	v_cvt_pk_bf16_f32 v10, v10, v11
	v_cvt_pk_bf16_f32 v11, v12, v13
	ds_write_b64 v162, v[10:11] offset:8192
	v_mfma_f32_16x16x32_bf16 v[106:109], v[242:245], v[86:89], v[118:121]
	v_mfma_f32_16x16x32_bf16 v[114:117], v[246:249], v[86:89], v[122:125]
	v_mfma_f32_16x16x32_bf16 v[10:13], v[166:169], v[86:89], v[126:129]
	s_waitcnt vmcnt(1)
	s_waitcnt lgkmcnt(3)
	v_mfma_f32_16x16x32_bf16 v[86:89], v[238:241], v[98:101], v[130:133]
	v_cvt_pk_bf16_f32 v6, v6, v7
	v_cvt_pk_bf16_f32 v7, v8, v9
	ds_write_b64 v162, v[6:7] offset:16384
	v_mfma_f32_16x16x32_bf16 v[118:121], v[242:245], v[98:101], v[134:137]
	v_mfma_f32_16x16x32_bf16 v[122:125], v[246:249], v[98:101], v[138:141]
	v_mfma_f32_16x16x32_bf16 v[6:9], v[166:169], v[98:101], v[142:145]
	s_waitcnt vmcnt(0)
	s_waitcnt lgkmcnt(2)
	v_mfma_f32_16x16x32_bf16 v[98:101], v[238:241], v[110:113], v[146:149]
	v_cvt_pk_bf16_f32 v2, v2, v3
	v_cvt_pk_bf16_f32 v3, v4, v5
	ds_write_b64 v162, v[2:3] offset:24576
	v_mfma_f32_16x16x32_bf16 v[126:129], v[242:245], v[110:113], v[150:153]
	v_mfma_f32_16x16x32_bf16 v[130:133], v[246:249], v[110:113], v[154:157]
	v_mfma_f32_16x16x32_bf16 v[2:5], v[166:169], v[110:113], v[158:161]
	s_waitcnt lgkmcnt(0)
	s_barrier
	v_add_u32_e32 v168, s56, v212
	v_add_u32_e32 v183, s56, v183
	v_add_u32_e32 v181, s56, v181
	ds_read_b64_tr_b16 v[110:111], v168
	ds_read_b64_tr_b16 v[112:113], v168 offset:2048
	ds_read_b64_tr_b16 v[134:135], v183
	ds_read_b64_tr_b16 v[136:137], v183 offset:2048
	ds_read_b128 v[138:141], v250 offset:32768
	ds_read_b64_tr_b16 v[142:143], v181
	ds_read_b128 v[146:149], v250 offset:34816
	ds_read_b128 v[150:153], v250 offset:36864
	ds_read_b64_tr_b16 v[144:145], v181 offset:2048
	v_add_u32_e32 v172, s56, v172
	ds_read_b64_tr_b16 v[154:155], v172
	ds_read_b64_tr_b16 v[156:157], v172 offset:2048
	s_waitcnt lgkmcnt(6)
	v_mfma_f32_16x16x32_bf16 v[62:65], v[110:113], v[138:141], v[62:65]
	v_mfma_f32_16x16x32_bf16 v[58:61], v[134:137], v[138:141], v[58:61]
	s_waitcnt lgkmcnt(2)
	v_mfma_f32_16x16x32_bf16 v[54:57], v[142:145], v[138:141], v[54:57]
	s_waitcnt lgkmcnt(0)
	v_mfma_f32_16x16x32_bf16 v[30:33], v[154:157], v[138:141], v[30:33]
	v_mfma_f32_16x16x32_bf16 v[42:45], v[110:113], v[146:149], v[42:45]
	ds_read_b128 v[138:141], v250 offset:38912
	v_mfma_f32_16x16x32_bf16 v[46:49], v[134:137], v[146:149], v[46:49]
	v_mfma_f32_16x16x32_bf16 v[38:41], v[142:145], v[146:149], v[38:41]
	v_mfma_f32_16x16x32_bf16 v[26:29], v[154:157], v[146:149], v[26:29]
	v_mfma_f32_16x16x32_bf16 v[34:37], v[110:113], v[150:153], v[34:37]
	ds_read_b128 v[146:149], v250 offset:40960
	v_mfma_f32_16x16x32_bf16 v[66:69], v[134:137], v[150:153], v[66:69]
	v_mfma_f32_16x16x32_bf16 v[74:77], v[142:145], v[150:153], v[74:77]
	v_mfma_f32_16x16x32_bf16 v[22:25], v[154:157], v[150:153], v[22:25]
	s_waitcnt lgkmcnt(1)
	v_mfma_f32_16x16x32_bf16 v[150:153], v[134:137], v[138:141], v[82:85]
	s_nop 2
	ds_read_b128 v[82:85], v250 offset:43008
	v_mfma_f32_16x16x32_bf16 v[78:81], v[110:113], v[138:141], v[78:81]
	v_mfma_f32_16x16x32_bf16 v[18:21], v[154:157], v[138:141], v[18:21]
	v_mfma_f32_16x16x32_bf16 v[158:161], v[142:145], v[138:141], v[90:93]
	s_nop 2
	ds_read_b128 v[90:93], v250 offset:45056
	ds_read_b64_tr_b16 v[166:167], v168 offset:16384
	ds_read_b64_tr_b16 v[168:169], v168 offset:18432
	s_waitcnt lgkmcnt(4)
	v_mfma_f32_16x16x32_bf16 v[50:53], v[110:113], v[146:149], v[50:53]
	v_mfma_f32_16x16x32_bf16 v[14:17], v[154:157], v[146:149], v[14:17]
	v_mfma_f32_16x16x32_bf16 v[138:141], v[134:137], v[146:149], v[94:97]
	v_mfma_f32_16x16x32_bf16 v[162:165], v[142:145], v[146:149], v[102:105]
	s_waitcnt lgkmcnt(3)
	v_mfma_f32_16x16x32_bf16 v[146:149], v[110:113], v[82:85], v[70:73]
	s_nop 2
	ds_read_b128 v[70:73], v250 offset:47104
	ds_read_b64_tr_b16 v[220:221], v183 offset:16384
	ds_read_b64_tr_b16 v[222:223], v183 offset:18432
	v_mfma_f32_16x16x32_bf16 v[10:13], v[154:157], v[82:85], v[10:13]
	v_mfma_f32_16x16x32_bf16 v[212:215], v[134:137], v[82:85], v[106:109]
	v_mfma_f32_16x16x32_bf16 v[216:219], v[142:145], v[82:85], v[114:117]
	ds_read_b128 v[82:85], v200 offset:32768
	ds_read_b64_tr_b16 v[236:237], v181 offset:16384
	ds_read_b64_tr_b16 v[238:239], v181 offset:18432
	s_waitcnt lgkmcnt(8)
	v_mfma_f32_16x16x32_bf16 v[6:9], v[154:157], v[90:93], v[6:9]
	v_mfma_f32_16x16x32_bf16 v[224:227], v[110:113], v[90:93], v[86:89]
	v_mfma_f32_16x16x32_bf16 v[228:231], v[134:137], v[90:93], v[118:121]
	v_mfma_f32_16x16x32_bf16 v[232:235], v[142:145], v[90:93], v[122:125]
	s_waitcnt lgkmcnt(5)
	v_mfma_f32_16x16x32_bf16 v[130:133], v[142:145], v[70:73], v[130:133]
	ds_read_b128 v[86:89], v200 offset:34816
	ds_read_b64_tr_b16 v[142:143], v172 offset:16384
	ds_read_b64_tr_b16 v[144:145], v172 offset:18432
	v_mfma_f32_16x16x32_bf16 v[240:243], v[110:113], v[70:73], v[98:101]
	v_mfma_f32_16x16x32_bf16 v[134:137], v[134:137], v[70:73], v[126:129]
	v_mfma_f32_16x16x32_bf16 v[154:157], v[154:157], v[70:73], v[2:5]
	s_nop 2
	ds_read_b128 v[2:5], v200 offset:36864
	s_waitcnt lgkmcnt(6)
	v_mfma_f32_16x16x32_bf16 v[122:125], v[166:169], v[82:85], v[62:65]
	v_mfma_f32_16x16x32_bf16 v[114:117], v[220:223], v[82:85], v[58:61]
	s_waitcnt lgkmcnt(4)
	v_mfma_f32_16x16x32_bf16 v[126:129], v[236:239], v[82:85], v[54:57]
	s_waitcnt lgkmcnt(1)
	v_mfma_f32_16x16x32_bf16 v[118:121], v[142:145], v[82:85], v[30:33]
	s_nop 2
	ds_read_b128 v[30:33], v200 offset:38912
	v_mfma_f32_16x16x32_bf16 v[106:109], v[166:169], v[86:89], v[42:45]
	v_mfma_f32_16x16x32_bf16 v[98:101], v[220:223], v[86:89], v[46:49]
	v_mfma_f32_16x16x32_bf16 v[110:113], v[236:239], v[86:89], v[38:41]
	v_mfma_f32_16x16x32_bf16 v[102:105], v[142:145], v[86:89], v[26:29]
	s_nop 2
	ds_read_b128 v[26:29], v200 offset:40960
	s_waitcnt lgkmcnt(2)
	v_mfma_f32_16x16x32_bf16 v[90:93], v[166:169], v[2:5], v[34:37]
	v_mfma_f32_16x16x32_bf16 v[82:85], v[220:223], v[2:5], v[66:69]
	v_mfma_f32_16x16x32_bf16 v[94:97], v[236:239], v[2:5], v[74:77]
	v_mfma_f32_16x16x32_bf16 v[86:89], v[142:145], v[2:5], v[22:25]
	ds_read_b128 v[2:5], v200 offset:43008
	s_waitcnt lgkmcnt(2)
	v_mfma_f32_16x16x32_bf16 v[74:77], v[166:169], v[30:33], v[78:81]
	v_mfma_f32_16x16x32_bf16 v[66:69], v[220:223], v[30:33], v[150:153]
	v_mfma_f32_16x16x32_bf16 v[78:81], v[236:239], v[30:33], v[158:161]
	v_mfma_f32_16x16x32_bf16 v[70:73], v[142:145], v[30:33], v[18:21]
	ds_read_b128 v[22:25], v200 offset:45056
	s_waitcnt lgkmcnt(2)
	v_mfma_f32_16x16x32_bf16 v[58:61], v[166:169], v[26:29], v[50:53]
	v_mfma_f32_16x16x32_bf16 v[50:53], v[220:223], v[26:29], v[138:141]
	v_mfma_f32_16x16x32_bf16 v[62:65], v[236:239], v[26:29], v[162:165]
	v_mfma_f32_16x16x32_bf16 v[54:57], v[142:145], v[26:29], v[14:17]
	s_waitcnt lgkmcnt(1)
	v_mfma_f32_16x16x32_bf16 v[42:45], v[166:169], v[2:5], v[146:149]
	ds_read_b128 v[138:141], v200 offset:47104
	v_mfma_f32_16x16x32_bf16 v[34:37], v[220:223], v[2:5], v[212:215]
	v_mfma_f32_16x16x32_bf16 v[46:49], v[236:239], v[2:5], v[216:219]
	v_mfma_f32_16x16x32_bf16 v[38:41], v[142:145], v[2:5], v[10:13]
	s_waitcnt lgkmcnt(1)
	v_mfma_f32_16x16x32_bf16 v[26:29], v[166:169], v[22:25], v[224:227]
	v_mfma_f32_16x16x32_bf16 v[18:21], v[220:223], v[22:25], v[228:231]
	v_mfma_f32_16x16x32_bf16 v[30:33], v[236:239], v[22:25], v[232:235]
	v_mfma_f32_16x16x32_bf16 v[22:25], v[142:145], v[22:25], v[6:9]
	s_waitcnt lgkmcnt(0)
	v_mfma_f32_16x16x32_bf16 v[10:13], v[166:169], v[138:141], v[240:243]
	v_mfma_f32_16x16x32_bf16 v[2:5], v[220:223], v[138:141], v[134:137]
	v_mfma_f32_16x16x32_bf16 v[14:17], v[236:239], v[138:141], v[130:133]
	v_mfma_f32_16x16x32_bf16 v[6:9], v[142:145], v[138:141], v[154:157]
	s_waitcnt lgkmcnt(0)
	s_barrier
	s_nop 0
	v_mov_b32_e32 v130, 0
	s_and_b64 vcc, exec, s[6:7]
	v_mov_b32_e32 v131, 0
	v_mov_b32_e32 v132, 0
	s_cbranch_vccnz .LBB0_1436
	global_load_dword v130, v[184:185], off
	global_load_dword v131, v[186:187], off
	global_load_dword v132, v[188:189], off
